# baseline (speedup 1.0000x reference)
_Z9ssim_mainPKfS0_S0_Pf:
	v_readfirstlane_b32 s29, v0
	s_load_dwordx4 s[4:7], s[0:1], 0x0
	s_load_dwordx4 s[8:11], s[0:1], 0x10
	s_mov_b32 s51, 0x44800000
	s_mov_b32 s38, 0
	s_mov_b32 s39, -1
	s_lshr_b32 s12, s29, 6
	s_and_b32 s13, s2, 7
	s_lshl_b32 s13, s13, 5
	s_lshr_b32 s14, s2, 3
	s_add_u32 s13, s13, s14
	s_lshr_b32 s14, s13, 3
	s_and_b32 s15, s13, 7
	s_lshl_b32 s16, s14, 20
	s_lshl_b32 s17, s15, 17
	s_add_u32 s16, s16, s17
	s_lshl_b32 s17, s12, 8
	s_add_u32 s16, s16, s17
	s_lshl_b32 s27, s12, 2
	s_add_u32 s27, s27, 0x10000
	v_and_b32_e32 v8, 63, v0
	v_and_b32_e32 v169, 15, v0
	v_bfe_u32 v164, v0, 4, 2
	v_lshrrev_b32_e32 v167, 2, v169
	v_lshlrev_b32_e32 v167, 5, v167
	v_and_b32_e32 v168, 1, v169
	v_lshl_or_b32 v167, v168, 4, v167
	v_bfe_u32 v168, v169, 1, 1
	v_lshl_or_b32 v167, v168, 7, v167
	v_lshl_or_b32 v9, v164, 14, v167
	v_and_b32_e32 v168, 1, v164
	v_lshl_or_b32 v23, v168, 14, v167
	v_lshrrev_b32_e32 v168, 1, v164
	v_lshl_or_b32 v23, v168, 13, v23
	v_add_u32_e32 v237, 0x1000, v9
	v_add_u32_e32 v238, 0x2000, v9
	v_add_u32_e32 v239, 0x3000, v9
	v_add_u32_e32 v240, 0x10000, v9
	v_add_u32_e32 v241, 0x11000, v9
	v_add_u32_e32 v242, 0x12000, v9
	v_add_u32_e32 v243, 0x13000, v9
	s_waitcnt lgkmcnt(0)
	s_load_dwordx8 s[40:47], s[8:9], 0x0
	s_load_dwordx2 s[48:49], s[8:9], 0x20
	s_load_dword s50, s[8:9], 0x28
	s_add_u32 s18, s4, s16
	s_addc_u32 s19, s5, 0
	s_add_u32 s20, s6, s16
	s_addc_u32 s21, s7, 0
	global_load_dwordx4 v[36:39], v9, s[18:19] offset:0 sc1 nt
	global_load_dwordx4 v[40:43], v9, s[18:19] offset:2048 sc1 nt
	global_load_dwordx4 v[68:71], v9, s[20:21] offset:0 sc1 nt
	global_load_dwordx4 v[72:75], v9, s[20:21] offset:2048 sc1 nt
	global_load_dwordx4 v[44:47], v237, s[18:19] offset:0 sc1 nt
	global_load_dwordx4 v[48:51], v237, s[18:19] offset:2048 sc1 nt
	global_load_dwordx4 v[76:79], v237, s[20:21] offset:0 sc1 nt
	global_load_dwordx4 v[80:83], v237, s[20:21] offset:2048 sc1 nt
	global_load_dwordx4 v[52:55], v238, s[18:19] offset:0 sc1 nt
	global_load_dwordx4 v[56:59], v238, s[18:19] offset:2048 sc1 nt
	global_load_dwordx4 v[84:87], v238, s[20:21] offset:0 sc1 nt
	global_load_dwordx4 v[88:91], v238, s[20:21] offset:2048 sc1 nt
	global_load_dwordx4 v[60:63], v239, s[18:19] offset:0 sc1 nt
	global_load_dwordx4 v[64:67], v239, s[18:19] offset:2048 sc1 nt
	global_load_dwordx4 v[92:95], v239, s[20:21] offset:0 sc1 nt
	global_load_dwordx4 v[96:99], v239, s[20:21] offset:2048 sc1 nt
	v_mov_b32_e32 v6, s27
	v_mov_b32_e32 v168, 0
	ds_write_b32 v6, v168 offset:0
	ds_write_b32 v6, v168 offset:32
	ds_write_b32 v6, v168 offset:64
	ds_write_b32 v6, v168 offset:96
	v_lshlrev_b32_e32 v167, 3, v164
	v_xor_b32_e32 v168, 16, v167
	v_sub_u32_e32 v165, v167, v169
	v_sub_u32_e32 v166, v168, v169
	v_add_u32_e32 v172, 0, v165
	v_min_u32_e32 v172, 11, v172
	v_lshlrev_b32_e32 v172, 2, v172
	v_add_u32_e32 v173, 1, v165
	v_min_u32_e32 v173, 11, v173
	v_lshlrev_b32_e32 v173, 2, v173
	v_add_u32_e32 v174, 2, v165
	v_min_u32_e32 v174, 11, v174
	v_lshlrev_b32_e32 v174, 2, v174
	v_add_u32_e32 v175, 3, v165
	v_min_u32_e32 v175, 11, v175
	v_lshlrev_b32_e32 v175, 2, v175
	v_add_u32_e32 v176, 4, v165
	v_min_u32_e32 v176, 11, v176
	v_lshlrev_b32_e32 v176, 2, v176
	v_add_u32_e32 v177, 5, v165
	v_min_u32_e32 v177, 11, v177
	v_lshlrev_b32_e32 v177, 2, v177
	v_add_u32_e32 v178, 6, v165
	v_min_u32_e32 v178, 11, v178
	v_lshlrev_b32_e32 v178, 2, v178
	v_add_u32_e32 v179, 7, v165
	v_min_u32_e32 v179, 11, v179
	v_lshlrev_b32_e32 v179, 2, v179
	v_add_u32_e32 v180, 0, v166
	v_min_u32_e32 v180, 11, v180
	v_lshlrev_b32_e32 v180, 2, v180
	v_add_u32_e32 v181, 1, v166
	v_min_u32_e32 v181, 11, v181
	v_lshlrev_b32_e32 v181, 2, v181
	v_add_u32_e32 v182, 2, v166
	v_min_u32_e32 v182, 11, v182
	v_lshlrev_b32_e32 v182, 2, v182
	v_add_u32_e32 v183, 3, v166
	v_min_u32_e32 v183, 11, v183
	v_lshlrev_b32_e32 v183, 2, v183
	v_add_u32_e32 v184, 4, v166
	v_min_u32_e32 v184, 11, v184
	v_lshlrev_b32_e32 v184, 2, v184
	v_add_u32_e32 v185, 5, v166
	v_min_u32_e32 v185, 11, v185
	v_lshlrev_b32_e32 v185, 2, v185
	v_add_u32_e32 v186, 6, v166
	v_min_u32_e32 v186, 11, v186
	v_lshlrev_b32_e32 v186, 2, v186
	v_add_u32_e32 v187, 7, v166
	v_min_u32_e32 v187, 11, v187
	v_lshlrev_b32_e32 v187, 2, v187
	s_cmp_eq_u32 s15, 7
	s_cselect_b32 s22, 0, 0x20000
	s_add_u32 s84, s18, s22
	s_addc_u32 s85, s19, 0
	s_add_u32 s86, s18, s22
	s_addc_u32 s87, s19, 0
	s_add_u32 s86, s86, 0x1000
	s_addc_u32 s87, s87, 0
	s_add_u32 s88, s20, s22
	s_addc_u32 s89, s21, 0
	s_add_u32 s90, s20, s22
	s_addc_u32 s91, s21, 0
	s_add_u32 s90, s90, 0x1000
	s_addc_u32 s91, s91, 0
	s_waitcnt lgkmcnt(0)
	v_writelane_b32 v171, s40, 0
	v_writelane_b32 v171, s41, 1
	v_writelane_b32 v171, s42, 2
	v_writelane_b32 v171, s43, 3
	v_writelane_b32 v171, s44, 4
	v_writelane_b32 v171, s45, 5
	v_writelane_b32 v171, s46, 6
	v_writelane_b32 v171, s47, 7
	v_writelane_b32 v171, s48, 8
	v_writelane_b32 v171, s49, 9
	v_writelane_b32 v171, s50, 10
	v_writelane_b32 v171, 0, 11
	v_fma_mixlo_f16 v171, v171, s51, 0
	ds_bpermute_b32 v188, v172, v171
	ds_bpermute_b32 v189, v173, v171
	ds_bpermute_b32 v190, v174, v171
	ds_bpermute_b32 v191, v175, v171
	ds_bpermute_b32 v192, v176, v171
	ds_bpermute_b32 v193, v177, v171
	ds_bpermute_b32 v194, v178, v171
	ds_bpermute_b32 v195, v179, v171
	v_lshlrev_b32_e32 v167, 2, v164
	s_cmp_eq_u32 s12, 0
	s_cselect_b32 s23, 6, 64
	v_add_u32_e32 v168, 0, v167
	v_cmp_gt_u32_e32 vcc, s23, v168
	s_nop 1
	v_cndmask_b32_e64 v15, 0, 1.0, vcc
	v_add_u32_e32 v168, 1, v167
	v_cmp_gt_u32_e32 vcc, s23, v168
	s_nop 1
	v_cndmask_b32_e64 v16, 0, 1.0, vcc
	v_add_u32_e32 v168, 2, v167
	v_cmp_gt_u32_e32 vcc, s23, v168
	s_nop 1
	v_cndmask_b32_e64 v17, 0, 1.0, vcc
	v_add_u32_e32 v168, 3, v167
	v_cmp_gt_u32_e32 vcc, s23, v168
	s_nop 1
	v_cndmask_b32_e64 v18, 0, 1.0, vcc
	v_and_b32_e32 v167, 31, v8
	v_lshlrev_b32_e32 v167, 4, v167
	s_lshl_b32 s24, s12, 11
	s_add_i32 s25, s12, 7
	s_and_b32 s25, s25, 7
	s_lshl_b32 s26, s25, 11
	v_or_b32_e32 v4, s24, v167
	v_or_b32_e32 v5, s26, v167
	s_lshl_b32 s28, s25, 2
	s_add_u32 s28, s28, 0x10000
	v_mov_b32_e32 v7, s28
	v_mov_b32_e32 v19, 0
	v_mov_b32_e32 v20, 0
	v_mov_b32_e32 v21, 0
	v_mov_b32_e32 v22, 0
	s_waitcnt lgkmcnt(7)
	ds_bpermute_b32 v196, v180, v171
	ds_bpermute_b32 v197, v181, v171
	ds_bpermute_b32 v198, v182, v171
	ds_bpermute_b32 v199, v183, v171
	ds_bpermute_b32 v200, v184, v171
	ds_bpermute_b32 v201, v185, v171
	ds_bpermute_b32 v202, v186, v171
	ds_bpermute_b32 v203, v187, v171
	s_waitcnt lgkmcnt(0)
	v_cmp_lt_u32_e64 s[32:33], 31, v8
	v_cmp_gt_u32_e64 s[34:35], 32, v8
	v_pack_b32_f16 v24, v188, v189
	v_pack_b32_f16 v25, v190, v191
	v_pack_b32_f16 v26, v192, v193
	v_pack_b32_f16 v27, v194, v195
	v_pack_b32_f16 v167, v196, v197
	v_cndmask_b32_e64 v28, 0, v167, s[32:33]
	v_cndmask_b32_e64 v32, 0, v167, s[34:35]
	v_pack_b32_f16 v167, v198, v199
	v_cndmask_b32_e64 v29, 0, v167, s[32:33]
	v_cndmask_b32_e64 v33, 0, v167, s[34:35]
	v_pack_b32_f16 v167, v200, v201
	v_cndmask_b32_e64 v30, 0, v167, s[32:33]
	v_cndmask_b32_e64 v34, 0, v167, s[34:35]
	v_pack_b32_f16 v167, v202, v203
	v_cndmask_b32_e64 v31, 0, v167, s[32:33]
	v_cndmask_b32_e64 v35, 0, v167, s[34:35]
	s_waitcnt lgkmcnt(0)
	s_cmp_lt_u32 s12, 4
	s_cbranch_scc1 .Lq_noprio
	s_setprio 1
.Lq_noprio:
	s_waitcnt vmcnt(12)
	v_cvt_pk_f16_f32 v164, v36, v40
	v_cvt_pk_f16_f32 v180, v68, v72
	v_pk_add_f16 v164, v164, -0.5 op_sel_hi:[1,0]
	v_pk_add_f16 v180, v180, -0.5 op_sel_hi:[1,0]
	v_pk_mul_f16 v196, v180, v180
	v_pk_mul_f16 v212, v164, v180
	v_pk_fma_f16 v196, v164, v164, v196
	v_cvt_pk_f16_f32 v168, v37, v41
	v_cvt_pk_f16_f32 v184, v69, v73
	v_pk_add_f16 v168, v168, -0.5 op_sel_hi:[1,0]
	v_pk_add_f16 v184, v184, -0.5 op_sel_hi:[1,0]
	v_pk_mul_f16 v200, v184, v184
	v_pk_mul_f16 v216, v168, v184
	v_pk_fma_f16 v200, v168, v168, v200
	v_cvt_pk_f16_f32 v172, v38, v42
	v_cvt_pk_f16_f32 v188, v70, v74
	v_pk_add_f16 v172, v172, -0.5 op_sel_hi:[1,0]
	v_pk_add_f16 v188, v188, -0.5 op_sel_hi:[1,0]
	v_pk_mul_f16 v204, v188, v188
	v_pk_mul_f16 v220, v172, v188
	v_pk_fma_f16 v204, v172, v172, v204
	v_cvt_pk_f16_f32 v176, v39, v43
	v_cvt_pk_f16_f32 v192, v71, v75
	v_pk_add_f16 v176, v176, -0.5 op_sel_hi:[1,0]
	v_pk_add_f16 v192, v192, -0.5 op_sel_hi:[1,0]
	v_pk_mul_f16 v208, v192, v192
	v_pk_mul_f16 v224, v176, v192
	v_pk_fma_f16 v208, v176, v176, v208
	s_waitcnt vmcnt(8)
	v_cvt_pk_f16_f32 v165, v44, v48
	v_cvt_pk_f16_f32 v181, v76, v80
	v_pk_add_f16 v165, v165, -0.5 op_sel_hi:[1,0]
	v_pk_add_f16 v181, v181, -0.5 op_sel_hi:[1,0]
	v_pk_mul_f16 v197, v181, v181
	v_pk_mul_f16 v213, v165, v181
	v_pk_fma_f16 v197, v165, v165, v197
	v_cvt_pk_f16_f32 v169, v45, v49
	v_cvt_pk_f16_f32 v185, v77, v81
	v_pk_add_f16 v169, v169, -0.5 op_sel_hi:[1,0]
	v_pk_add_f16 v185, v185, -0.5 op_sel_hi:[1,0]
	v_pk_mul_f16 v201, v185, v185
	v_pk_mul_f16 v217, v169, v185
	v_pk_fma_f16 v201, v169, v169, v201
	v_cvt_pk_f16_f32 v173, v46, v50
	v_cvt_pk_f16_f32 v189, v78, v82
	v_pk_add_f16 v173, v173, -0.5 op_sel_hi:[1,0]
	v_pk_add_f16 v189, v189, -0.5 op_sel_hi:[1,0]
	v_pk_mul_f16 v205, v189, v189
	v_pk_mul_f16 v221, v173, v189
	v_pk_fma_f16 v205, v173, v173, v205
	v_cvt_pk_f16_f32 v177, v47, v51
	v_cvt_pk_f16_f32 v193, v79, v83
	v_pk_add_f16 v177, v177, -0.5 op_sel_hi:[1,0]
	v_pk_add_f16 v193, v193, -0.5 op_sel_hi:[1,0]
	v_pk_mul_f16 v209, v193, v193
	v_pk_mul_f16 v225, v177, v193
	v_pk_fma_f16 v209, v177, v177, v209
	s_waitcnt vmcnt(4)
	v_cvt_pk_f16_f32 v166, v52, v56
	v_cvt_pk_f16_f32 v182, v84, v88
	v_pk_add_f16 v166, v166, -0.5 op_sel_hi:[1,0]
	v_pk_add_f16 v182, v182, -0.5 op_sel_hi:[1,0]
	v_pk_mul_f16 v198, v182, v182
	v_pk_mul_f16 v214, v166, v182
	v_pk_fma_f16 v198, v166, v166, v198
	v_cvt_pk_f16_f32 v170, v53, v57
	v_cvt_pk_f16_f32 v186, v85, v89
	v_pk_add_f16 v170, v170, -0.5 op_sel_hi:[1,0]
	v_pk_add_f16 v186, v186, -0.5 op_sel_hi:[1,0]
	v_pk_mul_f16 v202, v186, v186
	v_pk_mul_f16 v218, v170, v186
	v_pk_fma_f16 v202, v170, v170, v202
	v_cvt_pk_f16_f32 v174, v54, v58
	v_cvt_pk_f16_f32 v190, v86, v90
	v_pk_add_f16 v174, v174, -0.5 op_sel_hi:[1,0]
	v_pk_add_f16 v190, v190, -0.5 op_sel_hi:[1,0]
	v_pk_mul_f16 v206, v190, v190
	v_pk_mul_f16 v222, v174, v190
	v_pk_fma_f16 v206, v174, v174, v206
	v_cvt_pk_f16_f32 v178, v55, v59
	v_cvt_pk_f16_f32 v194, v87, v91
	v_pk_add_f16 v178, v178, -0.5 op_sel_hi:[1,0]
	v_pk_add_f16 v194, v194, -0.5 op_sel_hi:[1,0]
	v_pk_mul_f16 v210, v194, v194
	v_pk_mul_f16 v226, v178, v194
	v_pk_fma_f16 v210, v178, v178, v210
	s_waitcnt vmcnt(0)
	v_cvt_pk_f16_f32 v167, v60, v64
	v_cvt_pk_f16_f32 v183, v92, v96
	v_pk_add_f16 v167, v167, -0.5 op_sel_hi:[1,0]
	v_pk_add_f16 v183, v183, -0.5 op_sel_hi:[1,0]
	v_pk_mul_f16 v199, v183, v183
	v_pk_mul_f16 v215, v167, v183
	v_pk_fma_f16 v199, v167, v167, v199
	v_cvt_pk_f16_f32 v171, v61, v65
	v_cvt_pk_f16_f32 v187, v93, v97
	v_pk_add_f16 v171, v171, -0.5 op_sel_hi:[1,0]
	v_pk_add_f16 v187, v187, -0.5 op_sel_hi:[1,0]
	v_pk_mul_f16 v203, v187, v187
	v_pk_mul_f16 v219, v171, v187
	v_pk_fma_f16 v203, v171, v171, v203
	v_cvt_pk_f16_f32 v175, v62, v66
	v_cvt_pk_f16_f32 v191, v94, v98
	v_pk_add_f16 v175, v175, -0.5 op_sel_hi:[1,0]
	v_pk_add_f16 v191, v191, -0.5 op_sel_hi:[1,0]
	v_pk_mul_f16 v207, v191, v191
	v_pk_mul_f16 v223, v175, v191
	v_pk_fma_f16 v207, v175, v175, v207
	v_cvt_pk_f16_f32 v179, v63, v67
	v_cvt_pk_f16_f32 v195, v95, v99
	v_pk_add_f16 v179, v179, -0.5 op_sel_hi:[1,0]
	v_pk_add_f16 v195, v195, -0.5 op_sel_hi:[1,0]
	v_pk_mul_f16 v211, v195, v195
	v_pk_mul_f16 v227, v179, v195
	v_pk_fma_f16 v211, v179, v179, v211
	global_load_dwordx4 v[100:103], v240, s[18:19] offset:0 sc1 nt
	global_load_dwordx4 v[104:107], v240, s[18:19] offset:2048 sc1 nt
	global_load_dwordx4 v[132:135], v240, s[20:21] offset:0 sc1 nt
	global_load_dwordx4 v[136:139], v240, s[20:21] offset:2048 sc1 nt
	global_load_dwordx4 v[108:111], v241, s[18:19] offset:0 sc1 nt
	global_load_dwordx4 v[112:115], v241, s[18:19] offset:2048 sc1 nt
	global_load_dwordx4 v[140:143], v241, s[20:21] offset:0 sc1 nt
	global_load_dwordx4 v[144:147], v241, s[20:21] offset:2048 sc1 nt
	global_load_dwordx4 v[116:119], v242, s[18:19] offset:0 sc1 nt
	global_load_dwordx4 v[120:123], v242, s[18:19] offset:2048 sc1 nt
	global_load_dwordx4 v[148:151], v242, s[20:21] offset:0 sc1 nt
	global_load_dwordx4 v[152:155], v242, s[20:21] offset:2048 sc1 nt
	global_load_dwordx4 v[124:127], v243, s[18:19] offset:0 sc1 nt
	global_load_dwordx4 v[128:131], v243, s[18:19] offset:2048 sc1 nt
	global_load_dwordx4 v[156:159], v243, s[20:21] offset:0 sc1 nt
	global_load_dwordx4 v[160:163], v243, s[20:21] offset:2048 sc1 nt
	v_mfma_f32_16x16x32_f16 v[68:71], v[164:167], v[24:27], 0
	v_mfma_f32_16x16x32_f16 v[72:75], v[168:171], v[24:27], 0
	v_mfma_f32_16x16x32_f16 v[76:79], v[172:175], v[24:27], 0
	v_mfma_f32_16x16x32_f16 v[80:83], v[176:179], v[24:27], 0
	v_mfma_f32_16x16x32_f16 v[84:87], v[180:183], v[24:27], 0
	v_mfma_f32_16x16x32_f16 v[88:91], v[184:187], v[24:27], 0
	v_mfma_f32_16x16x32_f16 v[92:95], v[188:191], v[24:27], 0
	v_mfma_f32_16x16x32_f16 v[96:99], v[192:195], v[24:27], 0
	v_mov_b32_e32 v253, 0x44800000
	v_fma_mixlo_f16 v252, s40, v253, 0
	v_cvt_f32_f16_e32 v252, v252
	v_cvt_f64_f32_e32 v[236:237], v252
	v_add_f64 v[236:237], v[236:237], 0
	v_fma_mixlo_f16 v252, s41, v253, 0
	v_cvt_f32_f16_e32 v252, v252
	v_cvt_f64_f32_e32 v[238:239], v252
	v_add_f64 v[236:237], v[236:237], v[238:239]
	v_fma_mixlo_f16 v252, s42, v253, 0
	v_cvt_f32_f16_e32 v252, v252
	v_cvt_f64_f32_e32 v[238:239], v252
	v_add_f64 v[236:237], v[236:237], v[238:239]
	v_fma_mixlo_f16 v252, s43, v253, 0
	v_cvt_f32_f16_e32 v252, v252
	v_cvt_f64_f32_e32 v[238:239], v252
	v_add_f64 v[236:237], v[236:237], v[238:239]
	v_fma_mixlo_f16 v252, s44, v253, 0
	v_cvt_f32_f16_e32 v252, v252
	v_cvt_f64_f32_e32 v[238:239], v252
	v_add_f64 v[236:237], v[236:237], v[238:239]
	v_fma_mixlo_f16 v252, s45, v253, 0
	v_cvt_f32_f16_e32 v252, v252
	v_cvt_f64_f32_e32 v[238:239], v252
	v_add_f64 v[236:237], v[236:237], v[238:239]
	v_fma_mixlo_f16 v252, s46, v253, 0
	v_cvt_f32_f16_e32 v252, v252
	v_cvt_f64_f32_e32 v[238:239], v252
	v_add_f64 v[236:237], v[236:237], v[238:239]
	v_fma_mixlo_f16 v252, s47, v253, 0
	v_cvt_f32_f16_e32 v252, v252
	v_cvt_f64_f32_e32 v[238:239], v252
	v_add_f64 v[236:237], v[236:237], v[238:239]
	v_fma_mixlo_f16 v252, s48, v253, 0
	v_cvt_f32_f16_e32 v252, v252
	v_cvt_f64_f32_e32 v[238:239], v252
	v_add_f64 v[236:237], v[236:237], v[238:239]
	v_fma_mixlo_f16 v252, s49, v253, 0
	v_cvt_f32_f16_e32 v252, v252
	v_cvt_f64_f32_e32 v[238:239], v252
	v_add_f64 v[236:237], v[236:237], v[238:239]
	v_fma_mixlo_f16 v252, s50, v253, 0
	v_cvt_f32_f16_e32 v252, v252
	v_cvt_f64_f32_e32 v[238:239], v252
	v_add_f64 v[236:237], v[236:237], v[238:239]
	v_cvt_pk_f16_f32 v36, v68, v72
	v_cvt_pk_f16_f32 v37, v76, v80
	v_cvt_pk_f16_f32 v38, v69, v73
	v_cvt_pk_f16_f32 v39, v77, v81
	v_cvt_pk_f16_f32 v40, v70, v74
	v_cvt_pk_f16_f32 v41, v78, v82
	v_cvt_pk_f16_f32 v42, v71, v75
	v_cvt_pk_f16_f32 v43, v79, v83
	v_mfma_f32_16x16x32_f16 v[68:71], v[196:199], v[24:27], 0
	v_mfma_f32_16x16x32_f16 v[72:75], v[200:203], v[24:27], 0
	v_mfma_f32_16x16x32_f16 v[76:79], v[204:207], v[24:27], 0
	v_mfma_f32_16x16x32_f16 v[80:83], v[208:211], v[24:27], 0
	v_mul_f64 v[236:237], v[236:237], v[236:237]
	v_mul_f64 v[240:241], v[236:237], 0.5
	v_add_f64 v[242:243], v[240:241], v[240:241]
	s_mov_b32 s36, 0xeb1c432d
	s_mov_b32 s37, 0x3f1a36e2
	v_mul_f64 v[244:245], v[236:237], s[36:37]
	v_mul_f64 v[246:247], v[240:241], v[242:243]
	v_fmac_f64_e32 v[246:247], v[236:237], v[244:245]
	v_add_f64 v[248:249], v[236:237], v[236:237]
	s_mov_b32 s36, 0x487fcb92
	s_mov_b32 s37, 0x3f4d7dbf
	v_mul_f64 v[250:251], v[236:237], s[36:37]
	v_cvt_f32_f64_e32 v0, v[250:251]
	v_mov_b32_e32 v1, v0
	v_mov_b32_e32 v2, v0
	v_mov_b32_e32 v3, v0
	v_cvt_f32_f64_e32 v10, v[242:243]
	v_cvt_f32_f64_e32 v11, v[246:247]
	v_cvt_f32_f64_e32 v12, v[236:237]
	v_cvt_f32_f64_e32 v13, v[248:249]
	v_mul_f64 v[250:251], v[236:237], v[250:251]
	v_cvt_f32_f64_e32 v14, v[250:251]
	v_cvt_pk_f16_f32 v44, v84, v88
	v_cvt_pk_f16_f32 v45, v92, v96
	v_cvt_pk_f16_f32 v46, v85, v89
	v_cvt_pk_f16_f32 v47, v93, v97
	v_cvt_pk_f16_f32 v48, v86, v90
	v_cvt_pk_f16_f32 v49, v94, v98
	v_cvt_pk_f16_f32 v50, v87, v91
	v_cvt_pk_f16_f32 v51, v95, v99
	v_mfma_f32_16x16x32_f16 v[84:87], v[212:215], v[24:27], 0
	v_mfma_f32_16x16x32_f16 v[88:91], v[216:219], v[24:27], 0
	v_mfma_f32_16x16x32_f16 v[92:95], v[220:223], v[24:27], 0
	v_mfma_f32_16x16x32_f16 v[96:99], v[224:227], v[24:27], 0
	v_cvt_pk_f16_f32 v52, v68, v72
	v_cvt_pk_f16_f32 v53, v76, v80
	v_cvt_pk_f16_f32 v54, v69, v73
	v_cvt_pk_f16_f32 v55, v77, v81
	v_cvt_pk_f16_f32 v56, v70, v74
	v_cvt_pk_f16_f32 v57, v78, v82
	v_cvt_pk_f16_f32 v58, v71, v75
	v_cvt_pk_f16_f32 v59, v79, v83
	v_cvt_pk_f16_f32 v60, v84, v88
	v_cvt_pk_f16_f32 v61, v92, v96
	v_cvt_pk_f16_f32 v62, v85, v89
	v_cvt_pk_f16_f32 v63, v93, v97
	v_cvt_pk_f16_f32 v64, v86, v90
	v_cvt_pk_f16_f32 v65, v94, v98
	v_cvt_pk_f16_f32 v66, v87, v91
	v_cvt_pk_f16_f32 v67, v95, v99
	s_mov_b64 exec, s[38:39]
	ds_write_b128 v4, v[40:43] offset:0
	ds_write_b128 v4, v[48:51] offset:512
	ds_write_b128 v4, v[56:59] offset:1024
	ds_write_b128 v4, v[64:67] offset:1536
	s_mov_b64 exec, -1
	v_mfma_f32_16x16x32_f16 v[68:71], v[24:27], v[36:39], 0
	v_mfma_f32_16x16x32_f16 v[72:75], v[24:27], v[44:47], 0
	v_mfma_f32_16x16x32_f16 v[76:79], v[24:27], v[52:55], v[0:3]
	v_mfma_f32_16x16x32_f16 v[80:83], v[24:27], v[60:63], 0
	v_mfma_f32_16x16x32_f16 v[84:87], v[28:31], v[36:39], 0
	v_mfma_f32_16x16x32_f16 v[88:91], v[28:31], v[44:47], 0
	v_mfma_f32_16x16x32_f16 v[92:95], v[28:31], v[52:55], v[0:3]
	v_mfma_f32_16x16x32_f16 v[96:99], v[28:31], v[60:63], 0
	v_mfma_f32_16x16x32_f16 v[84:87], v[32:35], v[40:43], v[84:87]
	v_mfma_f32_16x16x32_f16 v[88:91], v[32:35], v[48:51], v[88:91]
	v_mfma_f32_16x16x32_f16 v[92:95], v[32:35], v[56:59], v[92:95]
	v_mfma_f32_16x16x32_f16 v[96:99], v[32:35], v[64:67], v[96:99]
	s_waitcnt lgkmcnt(0)
	ds_write_b32 v6, v6 offset:0
	ds_read_b32 v9, v7 offset:0
	v_mul_f32_e32 v244, v68, v72
	v_mul_f32_e32 v250, v69, v73
	v_mul_f32_e64 v245, -v72, v72
	v_mul_f32_e64 v251, -v73, v73
	v_add_f32_e32 v246, v68, v72
	v_add_f32_e32 v252, v69, v73
	v_fma_f32 v245, -v68, v68, v245
	v_fma_f32 v251, -v69, v69, v251
	v_fma_f32 v247, v10, v246, v11
	v_fma_f32 v253, v10, v252, v11
	v_fma_f32 v246, v13, v80, v14
	v_fma_f32 v252, v13, v81, v14
	v_fma_f32 v248, v12, v76, v245
	v_fma_f32 v254, v12, v77, v251
	v_fma_f32 v249, 2.0, v244, v247
	v_fma_f32 v255, 2.0, v250, v253
	v_sub_f32_e32 v247, v247, v245
	v_sub_f32_e32 v253, v253, v251
	v_fma_f32 v246, -2.0, v244, v246
	v_fma_f32 v252, -2.0, v250, v252
	v_mul_f32_e32 v247, v247, v248
	v_mul_f32_e32 v253, v253, v254
	v_rcp_f32_e32 v247, v247
	v_rcp_f32_e32 v253, v253
	v_mul_f32_e32 v249, v249, v246
	v_mul_f32_e32 v255, v255, v252
	v_fma_f32 v19, v249, v247, v19
	v_fma_f32 v19, v255, v253, v19
	v_mul_f32_e32 v244, v70, v74
	v_mul_f32_e32 v250, v71, v75
	v_mul_f32_e64 v245, -v74, v74
	v_mul_f32_e64 v251, -v75, v75
	v_add_f32_e32 v246, v70, v74
	v_add_f32_e32 v252, v71, v75
	v_fma_f32 v245, -v70, v70, v245
	v_fma_f32 v251, -v71, v71, v251
	v_fma_f32 v247, v10, v246, v11
	v_fma_f32 v253, v10, v252, v11
	v_fma_f32 v246, v13, v82, v14
	v_fma_f32 v252, v13, v83, v14
	v_fma_f32 v248, v12, v78, v245
	v_fma_f32 v254, v12, v79, v251
	v_fma_f32 v249, 2.0, v244, v247
	v_fma_f32 v255, 2.0, v250, v253
	v_sub_f32_e32 v247, v247, v245
	v_sub_f32_e32 v253, v253, v251
	v_fma_f32 v246, -2.0, v244, v246
	v_fma_f32 v252, -2.0, v250, v252
	v_mul_f32_e32 v247, v247, v248
	v_mul_f32_e32 v253, v253, v254
	v_rcp_f32_e32 v247, v247
	v_rcp_f32_e32 v253, v253
	v_mul_f32_e32 v249, v249, v246
	v_mul_f32_e32 v255, v255, v252
	v_fma_f32 v20, v249, v247, v20
	v_fma_f32 v20, v255, v253, v20
	v_mfma_f32_16x16x32_f16 v[68:71], v[24:27], v[40:43], 0
	v_mfma_f32_16x16x32_f16 v[72:75], v[24:27], v[48:51], 0
	v_mfma_f32_16x16x32_f16 v[76:79], v[24:27], v[56:59], v[0:3]
	v_mfma_f32_16x16x32_f16 v[80:83], v[24:27], v[64:67], 0
	s_barrier
	ds_read_b32 v9, v7 offset:0
	s_waitcnt lgkmcnt(0)
	v_cmp_ne_u32_e32 vcc, 0, v9
	s_cbranch_vccnz .Lq_go_0
